# v11: v10 + residual epilogues overlap second-half residual loads with first-half compute (counted wait)
# baseline (speedup 1.0000x reference)
; __device__ __forceinline__ u64_t* ssq_ptr(unsigned char* ws, int v) { return (u64_t*)(ws + CTL_SSQ) + (size_t)v * NTOK; }
; __device__ __forceinline__ u64_t ssq_fix(float ss) { return (u64_t)(ss * 16777216.0f); }
; #define ROW_FENCE() asm volatile("" ::: "memory")
; __device__ __forceinline__ u32x4 pack8(const f32x4& a, const f32x4& b) { u32x4 w; w.x = pk_bf16(a[0], a[1]); w.y = pk_bf16(a[2], a[3]); w.z = pk_bf16(b[0], b[1]); w.w = pk_bf16(b[2], b[3]); return w; }
;     __device__ __forceinline__ void operator()(const f32x4 (&acc)[2][2][4][2], const pg8::Unit& u, int wr, int wc, int fr, int fq) const {
;         bf16_t* xb = (bf16_t*)(ws + WS_XB); u64_t* ssq = ssq_ptr(ws, v);
;         float osc = 1.0f; if constexpr (SC) osc = __uint_as_float(((const unsigned*)(ws + CTL_AMAX))[AMAX_W2]) * (1.0f / 256.0f);
;         const int col = u.pn * 256 + wc * 32 + 8 * fq;
; #pragma unroll
;         for (int ai = 0; ai < 2; ++ai) {
;             u32x4 bs[4][2];
; #pragma unroll
;             for (int m = 0; m < 4; ++m) { const size_t off = (size_t)(u.pm * 256 + ai * 128 + wr * 64 + m * 16 + fr) * D + col;
; #pragma unroll
;                 for (int bj = 0; bj < 2; ++bj) bs[m][bj] = *(const u32x4*)(xb + off + bj * 128); }
;             ROW_FENCE();
; #pragma unroll
;             for (int m = 0; m < 4; ++m) {
;                 const int row = u.pm * 256 + ai * 128 + wr * 64 + m * 16 + fr; const size_t off = (size_t)row * D + col; float ss = 0.f;
;                 float rsc = osc; if constexpr (SC) asm volatile("" : "+v"(rsc));
; #pragma unroll
;                 for (int bj = 0; bj < 2; ++bj) { f32x4 b0, b1; unpack8(bs[m][bj], b0, b1); const f32x4 x0 = SC ? b0 + acc[ai][bj][m][0] * rsc : b0 + acc[ai][bj][m][0], x1 = SC ? b1 + acc[ai][bj][m][1] * rsc : b1 + acc[ai][bj][m][1];
;                     if (!dry) *(u32x4*)(xb + off + bj * 128) = pack8(x0, x1);
;                     ss += ((x0[0] * x0[0] + x0[1] * x0[1]) + (x0[2] * x0[2] + x0[3] * x0[3])) + ((x1[0] * x1[0] + x1[1] * x1[1]) + (x1[2] * x1[2] + x1[3] * x1[3])); }
;                 ss += __shfl_xor(ss, 16); ss += __shfl_xor(ss, 32);
;                 if (fq == 0 && !dry) atomicAdd(ssq + row, ssq_fix(ss));
;             }
.LBB0_1089:
	s_mov_b32 s11, s93
	v_and_b32_e32 v170, 64, v251
	v_mbcnt_lo_u32_b32 v130, -1, s11
	v_mbcnt_hi_u32_b32 v171, -1, v130
	s_lshl_b32 s11, s45, 8
	v_ashrrev_i32_e32 v130, 1, v171
	s_or_b32 s11, s11, s40
	v_and_b32_e32 v130, -8, v130
	v_add_u32_e32 v130, s11, v130
	s_lshl_b32 s11, s18, 8
	s_add_i32 s11, s11, s39
	v_and_or_b32 v156, v171, 15, s11
	v_ashrrev_i32_e32 v131, 31, v130
	v_ashrrev_i32_e32 v157, 31, v156
	v_lshl_add_u64 v[158:159], v[130:131], 1, s[6:7]
	v_lshlrev_b64 v[130:131], 11, v[156:157]
	v_lshl_add_u64 v[180:181], v[158:159], 0, v[130:131]
	flat_load_dwordx4 v[172:175], v[180:181]
	flat_load_dwordx4 v[176:179], v[180:181] offset:256
	v_or_b32_e32 v130, 16, v156
	v_or_b32_e32 v132, 32, v156
	v_or_b32_e32 v134, 48, v156
	v_ashrrev_i32_e32 v131, 31, v130
	v_ashrrev_i32_e32 v133, 31, v132
	v_ashrrev_i32_e32 v135, 31, v134
	v_lshlrev_b64 v[130:131], 11, v[130:131]
	v_lshlrev_b64 v[132:133], 11, v[132:133]
	v_lshlrev_b64 v[134:135], 11, v[134:135]
	v_lshl_add_u64 v[168:169], v[158:159], 0, v[130:131]
	v_lshl_add_u64 v[162:163], v[158:159], 0, v[132:133]
	v_lshl_add_u64 v[160:161], v[158:159], 0, v[134:135]
	flat_load_dwordx4 v[150:153], v[168:169]
	flat_load_dwordx4 v[146:149], v[168:169] offset:256
	flat_load_dwordx4 v[142:145], v[162:163]
	flat_load_dwordx4 v[138:141], v[162:163] offset:256
	flat_load_dwordx4 v[134:137], v[160:161]
	flat_load_dwordx4 v[130:133], v[160:161] offset:256
	v_mov_b32_e32 v246, 0x40000
	v_mov_b32_e32 v247, 0
	v_lshl_add_u64 v[238:239], v[180:181], 0, v[246:247]
	v_lshl_add_u64 v[240:241], v[168:169], 0, v[246:247]
	v_lshl_add_u64 v[242:243], v[162:163], 0, v[246:247]
	v_lshl_add_u64 v[244:245], v[160:161], 0, v[246:247]
	global_load_dwordx4 v[206:209], v[238:239], off
	global_load_dwordx4 v[210:213], v[238:239], off offset:256
	global_load_dwordx4 v[214:217], v[240:241], off
	global_load_dwordx4 v[218:221], v[240:241], off offset:256
	global_load_dwordx4 v[222:225], v[242:243], off
	global_load_dwordx4 v[226:229], v[242:243], off offset:256
	global_load_dwordx4 v[230:233], v[244:245], off
	global_load_dwordx4 v[234:237], v[244:245], off offset:256
	v_xor_b32_e32 v167, 16, v251
	v_add_u32_e32 v170, 64, v170
	v_xor_b32_e32 v182, 32, v251
	v_cmp_lt_i32_e32 vcc, v167, v170
	s_waitcnt vmcnt(8) lgkmcnt(0)
	v_and_b32_e32 v183, 0xffff0000, v172
	v_cndmask_b32_e32 v167, v251, v167, vcc
	v_cmp_lt_i32_e32 vcc, v182, v170
	v_lshlrev_b32_e32 v170, 2, v167
	v_lshlrev_b32_e32 v184, 16, v174
	v_cndmask_b32_e32 v182, v251, v182, vcc
	v_lshlrev_b32_e32 v167, 2, v182
	v_lshlrev_b32_e32 v182, 16, v172
	v_lshlrev_b32_e32 v172, 16, v173
	v_and_b32_e32 v173, 0xffff0000, v173
	v_and_b32_e32 v185, 0xffff0000, v174
	v_lshlrev_b32_e32 v174, 16, v175
	v_and_b32_e32 v175, 0xffff0000, v175
	v_lshlrev_b32_e32 v186, 16, v176
	v_and_b32_e32 v187, 0xffff0000, v176
	v_lshlrev_b32_e32 v176, 16, v177
	v_and_b32_e32 v177, 0xffff0000, v177
	v_lshlrev_b32_e32 v188, 16, v178
	v_and_b32_e32 v189, 0xffff0000, v178
	v_lshlrev_b32_e32 v178, 16, v179
	v_and_b32_e32 v179, 0xffff0000, v179
	v_pk_add_f32 v[128:129], v[128:129], v[172:173]
	v_pk_add_f32 v[126:127], v[126:127], v[182:183]
	v_pk_add_f32 v[124:125], v[124:125], v[174:175]
	v_pk_add_f32 v[122:123], v[122:123], v[184:185]
	v_pk_add_f32 v[120:121], v[120:121], v[176:177]
	v_pk_add_f32 v[118:119], v[118:119], v[186:187]
	v_pk_add_f32 v[172:173], v[116:117], v[178:179]
	v_pk_add_f32 v[174:175], v[114:115], v[188:189]
	v_cmp_gt_u32_e32 vcc, 16, v171
	v_cvt_pk_bf16_f32 v114, v126, v127
	v_cvt_pk_bf16_f32 v115, v128, v129
	v_mul_f32_e32 v116, v127, v127
	v_mul_f32_e32 v117, v129, v129
	v_mul_f32_e32 v127, v123, v123
	v_mul_f32_e32 v129, v125, v125
	v_mul_f32_e32 v171, v119, v119
	v_mul_f32_e32 v176, v121, v121
	v_mul_f32_e32 v177, v175, v175
	v_mul_f32_e32 v178, v173, v173
	v_fmac_f32_e32 v116, v126, v126
	v_fmac_f32_e32 v117, v128, v128
	v_fmac_f32_e32 v127, v122, v122
	v_fmac_f32_e32 v129, v124, v124
	v_fmac_f32_e32 v171, v118, v118
	v_fmac_f32_e32 v176, v120, v120
	v_fmac_f32_e32 v177, v174, v174
	v_fmac_f32_e32 v178, v172, v172
	v_add_f32_e32 v116, v116, v117
	v_add_f32_e32 v117, v127, v129
	v_add_f32_e32 v126, v171, v176
	v_add_f32_e32 v127, v177, v178
	v_add_f32_e32 v116, v116, v117
	v_add_f32_e32 v117, v126, v127
	v_add_f32_e32 v126, v116, v117
	ds_bpermute_b32 v127, v170, v126
	v_cvt_pk_bf16_f32 v116, v122, v123
	v_cvt_pk_bf16_f32 v117, v124, v125
	flat_store_dwordx4 v[180:181], v[114:117]
	s_waitcnt lgkmcnt(0)
	s_nop 0
	v_add_f32_e32 v114, v126, v127
	ds_bpermute_b32 v115, v167, v114
	v_cvt_pk_bf16_f32 v116, v118, v119
	v_cvt_pk_bf16_f32 v117, v120, v121
	v_cvt_pk_bf16_f32 v118, v174, v175
	v_cvt_pk_bf16_f32 v119, v172, v173
	flat_store_dwordx4 v[180:181], v[116:119] offset:256
	s_and_saveexec_b64 s[18:19], vcc
	s_cbranch_execz .LBB0_1091
	s_waitcnt lgkmcnt(0)
	v_add_f32_e32 v114, v114, v115
	v_mul_f32_e32 v114, 0x4b800000, v114
	v_trunc_f32_e32 v114, v114
	v_mul_f32_e32 v115, 0x2f800000, v114
	v_floor_f32_e32 v115, v115
	v_fmac_f32_e32 v114, 0xcf800000, v115
	v_cvt_u32_f32_e32 v114, v114
	v_cvt_u32_f32_e32 v115, v115
	v_lshl_add_u64 v[116:117], v[156:157], 3, s[8:9]
	flat_atomic_add_x2 v[116:117], v[114:115]

; __device__ __forceinline__ u64_t* ssq_ptr(unsigned char* ws, int v) { return (u64_t*)(ws + CTL_SSQ) + (size_t)v * NTOK; }
; __device__ __forceinline__ u64_t ssq_fix(float ss) { return (u64_t)(ss * 16777216.0f); }
; #define ROW_FENCE() asm volatile("" ::: "memory")
; __device__ __forceinline__ u32x4 pack8(const f32x4& a, const f32x4& b) { u32x4 w; w.x = pk_bf16(a[0], a[1]); w.y = pk_bf16(a[2], a[3]); w.z = pk_bf16(b[0], b[1]); w.w = pk_bf16(b[2], b[3]); return w; }
;     __device__ __forceinline__ void operator()(const f32x4 (&acc)[2][2][4][2], const pg8::Unit& u, int wr, int wc, int fr, int fq) const {
;         bf16_t* xb = (bf16_t*)(ws + WS_XB); u64_t* ssq = ssq_ptr(ws, v);
;         float osc = 1.0f; if constexpr (SC) osc = __uint_as_float(((const unsigned*)(ws + CTL_AMAX))[AMAX_W2]) * (1.0f / 256.0f);
;         const int col = u.pn * 256 + wc * 32 + 8 * fq;
; #pragma unroll
;         for (int ai = 0; ai < 2; ++ai) {
;             u32x4 bs[4][2];
; #pragma unroll
;             for (int m = 0; m < 4; ++m) { const size_t off = (size_t)(u.pm * 256 + ai * 128 + wr * 64 + m * 16 + fr) * D + col;
; #pragma unroll
;                 for (int bj = 0; bj < 2; ++bj) bs[m][bj] = *(const u32x4*)(xb + off + bj * 128); }
;             ROW_FENCE();
; #pragma unroll
;             for (int m = 0; m < 4; ++m) {
;                 const int row = u.pm * 256 + ai * 128 + wr * 64 + m * 16 + fr; const size_t off = (size_t)row * D + col; float ss = 0.f;
;                 float rsc = osc; if constexpr (SC) asm volatile("" : "+v"(rsc));
; #pragma unroll
;                 for (int bj = 0; bj < 2; ++bj) { f32x4 b0, b1; unpack8(bs[m][bj], b0, b1); const f32x4 x0 = SC ? b0 + acc[ai][bj][m][0] * rsc : b0 + acc[ai][bj][m][0], x1 = SC ? b1 + acc[ai][bj][m][1] * rsc : b1 + acc[ai][bj][m][1];
;                     if (!dry) *(u32x4*)(xb + off + bj * 128) = pack8(x0, x1);
;                     ss += ((x0[0] * x0[0] + x0[1] * x0[1]) + (x0[2] * x0[2] + x0[3] * x0[3])) + ((x1[0] * x1[0] + x1[1] * x1[1]) + (x1[2] * x1[2] + x1[3] * x1[3])); }
;                 ss += __shfl_xor(ss, 16); ss += __shfl_xor(ss, 32);
;                 if (fq == 0 && !dry) atomicAdd(ssq + row, ssq_fix(ss));
;             }
.LBB0_1840:
	s_mov_b32 s2, s93
	s_nop 0
	v_mbcnt_lo_u32_b32 v130, -1, s2
	v_mbcnt_hi_u32_b32 v132, -1, v130
	v_mov_b64_e32 v[130:131], s[12:13]
	flat_load_dword v130, v[130:131]
	s_lshl_b32 s2, s44, 8
	s_or_b32 s2, s2, s36
	v_cmp_gt_u32_e32 vcc, 16, v132
	s_waitcnt vmcnt(0) lgkmcnt(0)
	v_mul_f32_e32 v158, 0x3b800000, v130
	v_ashrrev_i32_e32 v130, 1, v132
	v_and_b32_e32 v130, -8, v130
	v_add_u32_e32 v130, s2, v130
	s_lshl_b32 s2, s43, 8
	s_add_i32 s2, s2, s35
	v_and_or_b32 v156, v132, 15, s2
	v_ashrrev_i32_e32 v131, 31, v130
	v_ashrrev_i32_e32 v157, 31, v156
	v_lshl_add_u64 v[160:161], v[130:131], 1, s[8:9]
	v_lshlrev_b64 v[130:131], 11, v[156:157]
	v_lshl_add_u64 v[166:167], v[160:161], 0, v[130:131]
	flat_load_dwordx4 v[172:175], v[166:167]
	flat_load_dwordx4 v[176:179], v[166:167] offset:256
	v_or_b32_e32 v130, 16, v156
	v_ashrrev_i32_e32 v131, 31, v130
	v_lshlrev_b64 v[130:131], 11, v[130:131]
	v_lshl_add_u64 v[170:171], v[160:161], 0, v[130:131]
	v_or_b32_e32 v130, 32, v156
	v_ashrrev_i32_e32 v131, 31, v130
	v_lshlrev_b64 v[130:131], 11, v[130:131]
	v_lshl_add_u64 v[168:169], v[160:161], 0, v[130:131]
	v_or_b32_e32 v130, 48, v156
	v_ashrrev_i32_e32 v131, 31, v130
	v_lshlrev_b64 v[130:131], 11, v[130:131]
	v_lshl_add_u64 v[162:163], v[160:161], 0, v[130:131]
	flat_load_dwordx4 v[150:153], v[170:171]
	flat_load_dwordx4 v[146:149], v[170:171] offset:256
	flat_load_dwordx4 v[142:145], v[168:169]
	flat_load_dwordx4 v[138:141], v[168:169] offset:256
	flat_load_dwordx4 v[134:137], v[162:163]
	flat_load_dwordx4 v[130:133], v[162:163] offset:256
	v_mov_b32_e32 v246, 0x40000
	v_mov_b32_e32 v247, 0
	v_lshl_add_u64 v[238:239], v[166:167], 0, v[246:247]
	v_lshl_add_u64 v[240:241], v[170:171], 0, v[246:247]
	v_lshl_add_u64 v[242:243], v[168:169], 0, v[246:247]
	v_lshl_add_u64 v[244:245], v[162:163], 0, v[246:247]
	global_load_dwordx4 v[206:209], v[238:239], off
	global_load_dwordx4 v[210:213], v[238:239], off offset:256
	global_load_dwordx4 v[214:217], v[240:241], off
	global_load_dwordx4 v[218:221], v[240:241], off offset:256
	global_load_dwordx4 v[222:225], v[242:243], off
	global_load_dwordx4 v[226:229], v[242:243], off offset:256
	global_load_dwordx4 v[230:233], v[244:245], off
	global_load_dwordx4 v[234:237], v[244:245], off offset:256
	v_mov_b32_e32 v180, v158
	s_waitcnt vmcnt(8) lgkmcnt(0)
	v_lshlrev_b32_e32 v182, 16, v172
	v_and_b32_e32 v183, 0xffff0000, v172
	v_lshlrev_b32_e32 v172, 16, v173
	v_and_b32_e32 v173, 0xffff0000, v173
	v_lshlrev_b32_e32 v184, 16, v174
	v_and_b32_e32 v185, 0xffff0000, v174
	v_lshlrev_b32_e32 v174, 16, v175
	v_and_b32_e32 v175, 0xffff0000, v175
	v_pk_fma_f32 v[128:129], v[128:129], v[180:181], v[172:173] op_sel_hi:[1,0,1]
	v_pk_fma_f32 v[126:127], v[126:127], v[180:181], v[182:183] op_sel_hi:[1,0,1]
	v_pk_fma_f32 v[172:173], v[124:125], v[180:181], v[174:175] op_sel_hi:[1,0,1]
	v_pk_fma_f32 v[174:175], v[122:123], v[180:181], v[184:185] op_sel_hi:[1,0,1]
	v_cvt_pk_bf16_f32 v122, v126, v127
	v_cvt_pk_bf16_f32 v123, v128, v129
	v_cvt_pk_bf16_f32 v124, v174, v175
	v_cvt_pk_bf16_f32 v125, v172, v173
	flat_store_dwordx4 v[166:167], v[122:125]
	s_nop 1
	v_mul_f32_e32 v122, v127, v127
	v_mul_f32_e32 v123, v129, v129
	v_fmac_f32_e32 v122, v126, v126
	v_fmac_f32_e32 v123, v128, v128
	v_add_f32_e32 v122, v122, v123
	v_mul_f32_e32 v123, v175, v175
	v_mul_f32_e32 v124, v173, v173
	v_fmac_f32_e32 v123, v174, v174
	v_fmac_f32_e32 v124, v172, v172
	v_add_f32_e32 v123, v123, v124
	v_add_f32_e32 v172, v122, v123
	v_lshlrev_b32_e32 v122, 16, v176
	v_and_b32_e32 v123, 0xffff0000, v176
	v_lshlrev_b32_e32 v124, 16, v177
	v_and_b32_e32 v125, 0xffff0000, v177
	v_lshlrev_b32_e32 v126, 16, v178
	v_and_b32_e32 v127, 0xffff0000, v178
	v_lshlrev_b32_e32 v128, 16, v179
	v_and_b32_e32 v129, 0xffff0000, v179
	v_pk_fma_f32 v[120:121], v[120:121], v[180:181], v[124:125] op_sel_hi:[1,0,1]
	v_pk_fma_f32 v[118:119], v[118:119], v[180:181], v[122:123] op_sel_hi:[1,0,1]
	v_pk_fma_f32 v[122:123], v[116:117], v[180:181], v[128:129] op_sel_hi:[1,0,1]
	v_pk_fma_f32 v[124:125], v[114:115], v[180:181], v[126:127] op_sel_hi:[1,0,1]
	v_cvt_pk_bf16_f32 v114, v118, v119
	v_cvt_pk_bf16_f32 v115, v120, v121
	v_cvt_pk_bf16_f32 v116, v124, v125
	v_cvt_pk_bf16_f32 v117, v122, v123
	flat_store_dwordx4 v[166:167], v[114:117] offset:256
	s_nop 1
	v_mul_f32_e32 v114, v119, v119
	v_mul_f32_e32 v115, v121, v121
	v_fmac_f32_e32 v114, v118, v118
	v_fmac_f32_e32 v115, v120, v120
	v_add_f32_e32 v114, v114, v115
	v_mul_f32_e32 v115, v125, v125
	v_mul_f32_e32 v116, v123, v123
	v_fmac_f32_e32 v115, v124, v124
	v_fmac_f32_e32 v116, v122, v122
	v_add_f32_e32 v115, v115, v116
	v_add_f32_e32 v114, v114, v115
	v_and_b32_e32 v116, 64, v251
	v_add_f32_e32 v115, v172, v114
	v_xor_b32_e32 v114, 16, v251
	v_add_u32_e32 v117, 64, v116
	v_cmp_lt_i32_e64 s[2:3], v114, v117
	s_nop 1
	v_cndmask_b32_e64 v114, v251, v114, s[2:3]
	v_lshlrev_b32_e32 v114, 2, v114
	ds_bpermute_b32 v116, v114, v115
	s_waitcnt lgkmcnt(0)
	v_add_f32_e32 v116, v115, v116
	v_xor_b32_e32 v115, 32, v251
	v_cmp_lt_i32_e64 s[2:3], v115, v117
	s_nop 1
	v_cndmask_b32_e64 v115, v251, v115, s[2:3]
	v_lshlrev_b32_e32 v115, 2, v115
	ds_bpermute_b32 v117, v115, v116
	s_and_saveexec_b64 s[2:3], vcc
	s_cbranch_execz .LBB0_1842
	s_waitcnt lgkmcnt(0)
	v_add_f32_e32 v116, v116, v117
	v_mul_f32_e32 v116, 0x4b800000, v116
	v_trunc_f32_e32 v116, v116
	v_mul_f32_e32 v117, 0x2f800000, v116
	v_floor_f32_e32 v117, v117
	v_fmac_f32_e32 v116, 0xcf800000, v117
	v_cvt_u32_f32_e32 v116, v116
	v_cvt_u32_f32_e32 v117, v117
	v_lshl_add_u64 v[118:119], v[156:157], 3, s[10:11]
	flat_atomic_add_x2 v[118:119], v[116:117]
